# SB attention: all 8 K-fragment LDS reads issued up front with counted lgkmcnt (were 4 just-in-time read/wait rounds); second-half V transposed reads issued with the first half into dead registers
# speedup vs baseline: 1.0100x; 1.0032x over previous
; #define LAS __attribute__((address_space(3)))
; __device__ __forceinline__ float ex2(float x) { return __builtin_amdgcn_exp2f(x); }
; __device__ __forceinline__ float lg2(float x) { return __builtin_amdgcn_logf(x); }
; __device__ __forceinline__ f32x16 mfma32(bf16x8 a, bf16x8 b, f32x16 c) { return __builtin_amdgcn_mfma_f32_32x32x16_bf16(a, b, c, 0, 0, 0); }
; #define SB_DMA(t, s) do { glds(ksrc + (size_t)(t) * 64 * INP, shm + (s) * KS_SB + wid * 1024); glds(vsrc + (size_t)(t) * 64 * INP, shm + SB_VOFF + (s) * VS + wid * 1024); } while (0)
; #define SB_WAITBAR() asm volatile("s_waitcnt vmcnt(4) lgkmcnt(0)\n\ts_barrier" ::: "memory")
; __device__ __forceinline__ void sb_unit(int b, int h, int qb, const bf16_t* __restrict__ PROJ, bf16_t* OCAT, float* SSQO, ldsp shm, volatile LAS unsigned* FL) {
;     ...
;         SB_WAITBAR();
;         if (step > 0) { if (FL[(step - 1) % 3] == 0xFFu) break; }
;         if (tid == 0) FL[(step + 1) % 3] = 0u;
;         SB_DMA(SB_TILE(step + 3), (step + 3) & 3);
;         if (t <= tdw && !wfin) {
;             const LAS unsigned char* kb = shm + (step & 3) * KS_SB + hi * 1024 + r32 * 16;
;             f32x16 z0 = f32x16{}, z1 = f32x16{};
; #pragma unroll
;             for (int d0 = 0; d0 < 4; ++d0) { const bf16x8 k0 = *(const LAS bf16x8*)(kb + d0 * 2048), k1 = *(const LAS bf16x8*)(kb + d0 * 2048 + 512);
;                 z0 = mfma32(k0, qr[d0], z0); z1 = mfma32(k1, qr[d0], z1); }
;             const bool diag = (t == tdw); const int kb0 = t * 64 + 4 * hi;
;             f32x16 l0, l1; float tot = 0.f;
; #pragma unroll
;             for (int r = 0; r < 16; ++r) { l0[r] = -lg2(1.0f + ex2(fminf(z0[r], 100.f))); l1[r] = -lg2(1.0f + ex2(fminf(z1[r], 100.f))); }
.LBB0_1055:
	s_or_b64 exec, exec, s[4:5]
	s_add_i32 s6, s34, s2
	s_max_i32 s8, s6, 0
	s_add_i32 s7, s3, 0x6000
	s_lshl_b64 s[4:5], s[8:9], 18
	s_and_b32 s7, s7, 0x6000
	v_lshl_add_u64 v[38:39], v[154:155], 0, s[4:5]
	s_add_i32 s7, s26, s7
	v_lshl_add_u64 v[38:39], v[38:39], 0, s[82:83]
	s_mov_b32 m0, s7
	s_add_i32 s6, s6, 3
	global_load_lds_dwordx4 v[38:39], off
	v_lshl_add_u64 v[38:39], v[156:157], 0, s[4:5]
	v_lshl_add_u64 v[38:39], v[38:39], 0, s[84:85]
	s_add_i32 m0, s7, 0x8000
	s_cmp_gt_i32 s6, s35
	global_load_lds_dwordx4 v[38:39], off
	s_cselect_b64 s[4:5], -1, 0
	s_or_b64 s[4:5], s[0:1], s[4:5]
	s_and_b64 vcc, exec, s[4:5]
	s_cbranch_vccnz .LBB0_1061
	s_and_b32 s8, s3, 0x6000
	v_add_u32_e32 v1, s8, v164
	ds_read_b128 v[38:41], v1
	ds_read_b128 v[42:45], v1 offset:512
	ds_read_b128 v[46:49], v1 offset:2048
	ds_read_b128 v[50:53], v1 offset:2560
	ds_read_b128 v[54:57], v1 offset:4096
	ds_read_b128 v[58:61], v1 offset:4608
	ds_read_b128 v[62:65], v1 offset:6144
	ds_read_b128 v[66:69], v1 offset:6656
	s_cmp_eq_u32 s27, s2
	s_cselect_b64 s[16:17], -1, 0
	s_cmp_lg_u32 s27, s2
	s_waitcnt lgkmcnt(6)
	v_mfma_f32_32x32x16_bf16 v[98:113], v[38:41], v[130:133], 0
	v_mfma_f32_32x32x16_bf16 v[82:97], v[42:45], v[130:133], 0
	s_waitcnt lgkmcnt(4)
	v_mfma_f32_32x32x16_bf16 v[82:97], v[50:53], v[134:137], v[82:97]
	v_mfma_f32_32x32x16_bf16 v[98:113], v[46:49], v[134:137], v[98:113]
	s_waitcnt lgkmcnt(2)
	v_mfma_f32_32x32x16_bf16 v[82:97], v[58:61], v[138:141], v[82:97]
	v_mfma_f32_32x32x16_bf16 v[98:113], v[54:57], v[138:141], v[98:113]
	s_waitcnt lgkmcnt(0)
	v_mfma_f32_32x32x16_bf16 v[82:97], v[66:69], v[142:145], v[82:97]
	v_mfma_f32_32x32x16_bf16 v[98:113], v[62:65], v[142:145], v[98:113]
	s_nop 10
	v_min_f32_e32 v2, 0x42c80000, v82
	v_exp_f32_e32 v2, v2
	v_min_f32_e32 v60, 0x42c80000, v94
	v_exp_f32_e32 v60, v60
	v_add_f32_e32 v2, 1.0, v2
	v_min_f32_e32 v37, 0x42c80000, v99
	v_exp_f32_e32 v37, v37
	v_min_f32_e32 v1, 0x42c80000, v98
	v_exp_f32_e32 v1, v1
	v_log_f32_e32 v52, v2
	v_add_f32_e32 v2, 1.0, v37
	v_log_f32_e32 v37, v2
	v_add_f32_e32 v1, 1.0, v1
	v_min_f32_e32 v2, 0x42c80000, v83
	v_log_f32_e32 v1, v1
	v_exp_f32_e32 v39, v2
	v_mov_b32_e32 v2, v1
	v_mov_b32_e32 v1, v37
	v_add_f32_e32 v37, 1.0, v39
	v_min_f32_e32 v38, 0x42c80000, v100
	v_min_f32_e32 v39, 0x42c80000, v84
	v_exp_f32_e32 v38, v38
	v_exp_f32_e32 v39, v39
	v_min_f32_e32 v59, 0x42c80000, v110
	v_exp_f32_e32 v59, v59
	v_add_f32_e32 v38, 1.0, v38
	v_add_f32_e32 v39, 1.0, v39
	v_log_f32_e32 v54, v38
	v_log_f32_e32 v56, v39
	v_add_f32_e32 v59, 1.0, v59
	v_log_f32_e32 v74, v59
	v_add_f32_e32 v59, 1.0, v60
	v_min_f32_e32 v60, 0x42c80000, v111
	v_min_f32_e32 v40, 0x42c80000, v101
	v_exp_f32_e32 v60, v60
	v_min_f32_e32 v61, 0x42c80000, v95
	v_log_f32_e32 v53, v37
	v_exp_f32_e32 v40, v40
	v_min_f32_e32 v38, 0x42c80000, v85
	v_min_f32_e32 v39, 0x42c80000, v102
	v_exp_f32_e32 v61, v61
	v_exp_f32_e32 v38, v38
	v_exp_f32_e32 v39, v39
	v_log_f32_e32 v76, v59
	v_add_f32_e32 v59, 1.0, v60
	v_add_f32_e32 v37, 1.0, v40
	v_log_f32_e32 v75, v59
	v_add_f32_e32 v59, 1.0, v61
	v_min_f32_e32 v60, 0x42c80000, v112
	v_add_f32_e32 v38, 1.0, v38
	v_add_f32_e32 v39, 1.0, v39
	v_min_f32_e32 v40, 0x42c80000, v86
	v_exp_f32_e32 v60, v60
	v_min_f32_e32 v61, 0x42c80000, v96
	v_log_f32_e32 v55, v37
	v_log_f32_e32 v57, v38
	v_log_f32_e32 v58, v39
	v_exp_f32_e32 v40, v40
	v_exp_f32_e32 v61, v61
	v_log_f32_e32 v77, v59
	v_add_f32_e32 v59, 1.0, v60
	v_add_f32_e32 v37, 1.0, v40
	v_log_f32_e32 v78, v59
	v_add_f32_e32 v59, 1.0, v61
	v_min_f32_e32 v60, 0x42c80000, v113
	v_min_f32_e32 v38, 0x42c80000, v103
	v_min_f32_e32 v39, 0x42c80000, v87
	v_min_f32_e32 v40, 0x42c80000, v104
	v_min_f32_e32 v41, 0x42c80000, v88
	v_min_f32_e32 v42, 0x42c80000, v105
	v_min_f32_e32 v43, 0x42c80000, v89
	v_min_f32_e32 v44, 0x42c80000, v106
	v_min_f32_e32 v45, 0x42c80000, v90
	v_min_f32_e32 v46, 0x42c80000, v107
	v_min_f32_e32 v47, 0x42c80000, v91
	v_min_f32_e32 v48, 0x42c80000, v108
	v_min_f32_e32 v49, 0x42c80000, v92
	v_min_f32_e32 v50, 0x42c80000, v109
	v_min_f32_e32 v51, 0x42c80000, v93
	v_exp_f32_e32 v60, v60
	v_min_f32_e32 v61, 0x42c80000, v97
	v_exp_f32_e32 v38, v38
	v_exp_f32_e32 v39, v39
	v_exp_f32_e32 v40, v40
	v_exp_f32_e32 v41, v41
	v_exp_f32_e32 v42, v42
	v_exp_f32_e32 v43, v43
	v_exp_f32_e32 v44, v44
	v_exp_f32_e32 v45, v45
	v_exp_f32_e32 v46, v46
	v_exp_f32_e32 v47, v47
	v_exp_f32_e32 v48, v48
	v_exp_f32_e32 v49, v49
	v_exp_f32_e32 v50, v50
	v_exp_f32_e32 v51, v51
	v_exp_f32_e32 v61, v61
	v_log_f32_e32 v80, v59
	v_add_f32_e32 v59, 1.0, v60
	v_add_f32_e32 v38, 1.0, v38
	v_add_f32_e32 v39, 1.0, v39
	v_add_f32_e32 v40, 1.0, v40
	v_add_f32_e32 v41, 1.0, v41
	v_add_f32_e32 v42, 1.0, v42
	v_add_f32_e32 v43, 1.0, v43
	v_add_f32_e32 v44, 1.0, v44
	v_add_f32_e32 v45, 1.0, v45
	v_add_f32_e32 v46, 1.0, v46
	v_add_f32_e32 v47, 1.0, v47
	v_add_f32_e32 v48, 1.0, v48
	v_add_f32_e32 v49, 1.0, v49
	v_add_f32_e32 v50, 1.0, v50
	v_add_f32_e32 v51, 1.0, v51
	v_log_f32_e32 v79, v59
	v_add_f32_e32 v59, 1.0, v61
	v_log_f32_e32 v60, v37
	v_log_f32_e32 v38, v38
	v_log_f32_e32 v61, v39
	v_log_f32_e32 v62, v40
	v_log_f32_e32 v64, v41
	v_log_f32_e32 v63, v42
	v_log_f32_e32 v65, v43
	v_log_f32_e32 v66, v44
	v_log_f32_e32 v68, v45
	v_log_f32_e32 v67, v46
	v_log_f32_e32 v69, v47
	v_log_f32_e32 v70, v48
	v_log_f32_e32 v72, v49
	v_log_f32_e32 v71, v50
	v_log_f32_e32 v73, v51
	v_log_f32_e32 v81, v59
	v_mov_b32_e32 v59, v38
	s_cbranch_scc1 .LBB0_1058
; __device__ __forceinline__ void sb_unit(int b, int h, int qb, const bf16_t* __restrict__ PROJ, bf16_t* OCAT, float* SSQO, ldsp shm, volatile LAS unsigned* FL) {
;     ...
;             if (diag) {
; #pragma unroll
;                 for (int r = 0; r < 16; ++r) { const int kk = kb0 + (r & 3) + 8 * (r >> 2); if (kk >= qabs) l0[r] = 0.f; if (kk + 32 >= qabs) l1[r] = 0.f; } }
	v_add_u32_e32 v166, s33, v165
	v_add_u32_e32 v167, 0xc0, v166
	v_add_u32_e32 v168, 0xe0, v166
	v_add_u32_e32 v169, 0xc1, v166
	v_add_u32_e32 v170, 0xe1, v166
	v_add_u32_e32 v171, 0xc2, v166
	v_add_u32_e32 v172, 0xe2, v166
	v_add_u32_e32 v173, 0xc3, v166
	v_add_u32_e32 v174, 0xe3, v166
	v_add_u32_e32 v175, 0xc8, v166
	v_add_u32_e32 v176, 0xe8, v166
	v_add_u32_e32 v177, 0xc9, v166
	v_add_u32_e32 v178, 0xe9, v166
	v_add_u32_e32 v179, 0xca, v166
	v_add_u32_e32 v180, 0xea, v166
	v_add_u32_e32 v181, 0xcb, v166
	v_add_u32_e32 v182, 0xeb, v166
	v_add_u32_e32 v183, 0xd0, v166
	v_add_u32_e32 v184, 0xf0, v166
	v_add_u32_e32 v185, 0xd1, v166
	v_add_u32_e32 v186, 0xf1, v166
	v_add_u32_e32 v187, 0xd2, v166
	v_add_u32_e32 v188, 0xf2, v166
	v_add_u32_e32 v189, 0xd3, v166
	v_add_u32_e32 v190, 0xf3, v166
	v_add_u32_e32 v191, 0xd8, v166
	v_add_u32_e32 v192, 0xf8, v166
	v_add_u32_e32 v193, 0xd9, v166
	v_add_u32_e32 v194, 0xf9, v166
	v_add_u32_e32 v195, 0xda, v166
	v_add_u32_e32 v196, 0xfa, v166
	v_add_u32_e32 v197, 0xdb, v166
	v_add_u32_e32 v166, 0xfb, v166
	v_cmp_lt_i32_e64 s[44:45], v167, v163
	v_cmp_lt_i32_e64 s[6:7], v168, v163
	v_cmp_lt_i32_e64 s[68:69], v169, v163
	v_cmp_lt_i32_e64 s[0:1], v170, v163
	v_cmp_lt_i32_e64 s[72:73], v171, v163
	v_cmp_lt_i32_e64 s[40:41], v172, v163
	v_cmp_lt_i32_e64 s[76:77], v173, v163
	v_cmp_lt_i32_e64 s[42:43], v174, v163
	v_cmp_lt_i32_e64 s[78:79], v175, v163
	v_cmp_lt_i32_e64 s[48:49], v176, v163
	v_cmp_lt_i32_e64 s[80:81], v177, v163
	v_cmp_lt_i32_e64 s[50:51], v178, v163
	v_cmp_lt_i32_e64 s[82:83], v179, v163
	v_cmp_lt_i32_e64 s[52:53], v180, v163
	v_cmp_lt_i32_e64 s[84:85], v181, v163
	v_cmp_lt_i32_e64 s[54:55], v182, v163
	v_cmp_lt_i32_e64 s[88:89], v183, v163
	v_cmp_lt_i32_e64 s[58:59], v184, v163
	v_cmp_lt_i32_e64 s[90:91], v185, v163
	v_cmp_lt_i32_e64 s[60:61], v186, v163
	v_cmp_lt_i32_e64 s[92:93], v187, v163
	v_cmp_lt_i32_e64 s[62:63], v188, v163
	v_cmp_lt_i32_e64 s[94:95], v189, v163
	v_cmp_lt_i32_e64 s[64:65], v190, v163
	v_cmp_lt_i32_e64 s[96:97], v191, v163
	v_cmp_lt_i32_e64 s[66:67], v192, v163
	v_cmp_lt_i32_e64 s[4:5], v193, v163
	v_cmp_lt_i32_e64 s[70:71], v194, v163
	v_cmp_lt_i32_e32 vcc, v195, v163
	v_cmp_lt_i32_e64 s[74:75], v196, v163
	v_cmp_lt_i32_e64 s[86:87], v197, v163
	v_cmp_lt_i32_e64 s[56:57], v166, v163
	s_nop 1
	s_or_b64 vcc, s[86:87], vcc
	v_cndmask_b32_e32 v78, 0, v78, vcc
	s_or_b64 vcc, vcc, s[4:5]
	v_cndmask_b32_e32 v75, 0, v75, vcc
	s_or_b64 vcc, vcc, s[96:97]
	v_cndmask_b32_e32 v74, 0, v74, vcc
	s_or_b64 vcc, vcc, s[94:95]
	v_cndmask_b32_e32 v71, 0, v71, vcc
	s_or_b64 vcc, vcc, s[92:93]
	v_cndmask_b32_e32 v70, 0, v70, vcc
	s_or_b64 vcc, vcc, s[90:91]
	v_cndmask_b32_e32 v67, 0, v67, vcc
	s_or_b64 vcc, vcc, s[88:89]
	v_cndmask_b32_e32 v66, 0, v66, vcc
	s_or_b64 vcc, vcc, s[84:85]
	v_cndmask_b32_e32 v63, 0, v63, vcc
	s_or_b64 vcc, vcc, s[82:83]
	v_cndmask_b32_e32 v62, 0, v62, vcc
	s_or_b64 vcc, vcc, s[80:81]
	v_cndmask_b32_e32 v59, 0, v59, vcc
	s_or_b64 vcc, vcc, s[78:79]
	v_cndmask_b32_e32 v58, 0, v58, vcc
	s_or_b64 vcc, vcc, s[76:77]
	v_cndmask_b32_e32 v55, 0, v55, vcc
	s_or_b64 vcc, vcc, s[72:73]
	v_cndmask_b32_e32 v54, 0, v54, vcc
	s_or_b64 vcc, vcc, s[68:69]
	v_cndmask_b32_e32 v1, 0, v1, vcc
	s_or_b64 vcc, vcc, s[44:45]
	v_cndmask_b32_e32 v2, 0, v2, vcc
	s_or_b64 vcc, s[56:57], s[74:75]
	v_cndmask_b32_e32 v80, 0, v80, vcc
	s_or_b64 vcc, vcc, s[70:71]
	v_cndmask_b32_e32 v77, 0, v77, vcc
	s_or_b64 vcc, vcc, s[66:67]
	v_cndmask_b32_e32 v76, 0, v76, vcc
	s_or_b64 vcc, vcc, s[64:65]
	v_cndmask_b32_e32 v73, 0, v73, vcc
	s_or_b64 vcc, vcc, s[62:63]
	v_cndmask_b32_e32 v72, 0, v72, vcc
	s_or_b64 vcc, vcc, s[60:61]
	v_cndmask_b32_e32 v69, 0, v69, vcc
	s_or_b64 vcc, vcc, s[58:59]
	v_cndmask_b32_e32 v68, 0, v68, vcc
	s_or_b64 vcc, vcc, s[54:55]
	v_cndmask_b32_e32 v65, 0, v65, vcc
	s_or_b64 vcc, vcc, s[52:53]
	v_cndmask_b32_e32 v64, 0, v64, vcc
	s_or_b64 vcc, vcc, s[50:51]
	v_cndmask_b32_e32 v61, 0, v61, vcc
	s_or_b64 vcc, vcc, s[48:49]
	v_cndmask_b32_e32 v60, 0, v60, vcc
	s_or_b64 vcc, vcc, s[42:43]
	v_cndmask_b32_e32 v57, 0, v57, vcc
	s_or_b64 vcc, vcc, s[40:41]
	v_cndmask_b32_e32 v56, 0, v56, vcc
	s_or_b64 vcc, vcc, s[0:1]
	v_cndmask_b32_e32 v53, 0, v53, vcc
	s_or_b64 vcc, vcc, s[6:7]
	v_cndmask_b32_e64 v79, 0, v79, s[86:87]
	v_cndmask_b32_e32 v52, 0, v52, vcc
	v_cndmask_b32_e64 v81, 0, v81, s[56:57]

; #define LAS __attribute__((address_space(3)))
; __device__ __forceinline__ f32x16 mfma32(bf16x8 a, bf16x8 b, f32x16 c) { return __builtin_amdgcn_mfma_f32_32x32x16_bf16(a, b, c, 0, 0, 0); }
; __device__ __forceinline__ s16x4 vtr(const LAS unsigned char* p) { return __builtin_bit_cast(s16x4, __builtin_amdgcn_ds_read_tr16_b64_v4i16((LAS v4i16_t*)p)); }
; __device__ __forceinline__ float swapsum(float m) { auto rr = __builtin_amdgcn_permlane32_swap(__float_as_uint(m), __float_as_uint(m), false, false); return __uint_as_float(rr[0]) + __uint_as_float(rr[1]); }
; __device__ __forceinline__ u32x4 packp(const f32x16& p, int b) { u32x4 w; w.x = cvt_pk_bf16(p[b], p[b + 1]); w.y = cvt_pk_bf16(p[b + 2], p[b + 3]); w.z = cvt_pk_bf16(p[b + 4], p[b + 5]); w.w = cvt_pk_bf16(p[b + 6], p[b + 7]); return w; }
; __device__ __forceinline__ void pv(f32x16 (&o)[2], const LAS unsigned char* vp, u32x4 pw0, u32x4 pw1, u32x4 pw2, u32x4 pw3) {
; #pragma unroll
;     for (int d0 = 0; d0 < 2; ++d0) {
;         s16x4 lo[4], hi4[4];
; #pragma unroll
;         for (int ks = 0; ks < 4; ++ks) { lo[ks] = vtr(vp + d0 * 4096 + ks * 1024); hi4[ks] = vtr(vp + d0 * 4096 + ks * 1024 + 512); }
;     ...
;         o[d0] = mfma32(__builtin_bit_cast(bf16x8, pw0), ATT_PK(0), o[d0]);
;         o[d0] = mfma32(__builtin_bit_cast(bf16x8, pw1), ATT_PK(1), o[d0]);
;         o[d0] = mfma32(__builtin_bit_cast(bf16x8, pw2), ATT_PK(2), o[d0]);
;         o[d0] = mfma32(__builtin_bit_cast(bf16x8, pw3), ATT_PK(3), o[d0]);
;     ...
;     }
; }
; __device__ __forceinline__ void sb_unit(int b, int h, int qb, const bf16_t* __restrict__ PROJ, bf16_t* OCAT, float* SSQO, ldsp shm, volatile LAS unsigned* FL) {
;     ...
;             pv(o, vp0 + (step & 3) * VS, packp(z0, 0), packp(z0, 8), packp(z1, 0), packp(z1, 8));
;             Lc += swapsum(tot);
;             wfin = __all(Lc <= SB_DONE) != 0;
.LBB0_1060:
	v_add_u32_e32 v99, s8, v162
	ds_read_b64_tr_b16 v[100:101], v99 offset:32768
	ds_read_b64_tr_b16 v[102:103], v99 offset:33280
	ds_read_b64_tr_b16 v[104:105], v99 offset:33792
	ds_read_b64_tr_b16 v[106:107], v99 offset:34304
	ds_read_b64_tr_b16 v[108:109], v99 offset:34816
	ds_read_b64_tr_b16 v[110:111], v99 offset:35328
	ds_read_b64_tr_b16 v[200:201], v99 offset:35840
	ds_read_b64_tr_b16 v[202:203], v99 offset:36352
	ds_read_b64_tr_b16 v[166:167], v99 offset:36864
	ds_read_b64_tr_b16 v[168:169], v99 offset:37376
	ds_read_b64_tr_b16 v[170:171], v99 offset:37888
	ds_read_b64_tr_b16 v[172:173], v99 offset:38400
	ds_read_b64_tr_b16 v[174:175], v99 offset:38912
	ds_read_b64_tr_b16 v[176:177], v99 offset:39424
	ds_read_b64_tr_b16 v[178:179], v99 offset:39936
	ds_read_b64_tr_b16 v[180:181], v99 offset:40448
	v_cvt_pk_bf16_f32 v114, v84, v83
	v_cvt_pk_bf16_f32 v115, v88, v87
	v_cvt_pk_bf16_f32 v116, v92, v91
	v_cvt_pk_bf16_f32 v117, v96, v95
	v_add_f32_e32 v2, v2, v52
	v_add_f32_e32 v1, v1, v53
	v_add_f32_e32 v52, v54, v56
	v_add_f32_e32 v1, v1, v2
	v_add_f32_e32 v53, v55, v57
	v_add_f32_e32 v1, v52, v1
	v_add_f32_e32 v54, v58, v60
	v_add_f32_e32 v1, v53, v1
	v_add_f32_e32 v55, v59, v61
	v_add_f32_e32 v1, v54, v1
	v_add_f32_e32 v56, v62, v64
	v_add_f32_e32 v1, v55, v1
	s_mov_b32 s0, 0x43160000
	s_movk_i32 s80, 0xff
	s_mov_b32 s81, 0x41000000
	s_mov_b64 s[82:83], 0x800
	s_mov_b64 s[84:85], 0xc00
	s_mov_b64 s[86:87], 0x70000
	s_mov_b64 s[88:89], 0x70080
	s_waitcnt lgkmcnt(8)
	v_mfma_f32_32x32x16_bf16 v[20:35], v[114:117], v[100:103], v[20:35]
	v_cvt_pk_bf16_f32 v118, v86, v85
	v_cvt_pk_bf16_f32 v119, v90, v89
	v_cvt_pk_bf16_f32 v120, v94, v93
	v_cvt_pk_bf16_f32 v121, v98, v97
	v_add_f32_e32 v57, v63, v65
	v_add_f32_e32 v1, v56, v1
	v_mfma_f32_32x32x16_bf16 v[20:35], v[118:121], v[104:107], v[20:35]
	v_cvt_pk_bf16_f32 v122, v38, v37
	v_cvt_pk_bf16_f32 v123, v42, v41
	v_cvt_pk_bf16_f32 v124, v46, v45
	v_cvt_pk_bf16_f32 v125, v50, v49
	v_add_f32_e32 v58, v66, v68
	v_add_f32_e32 v1, v57, v1
	v_mfma_f32_32x32x16_bf16 v[20:35], v[122:125], v[108:111], v[20:35]
	v_cvt_pk_bf16_f32 v126, v40, v39
	v_cvt_pk_bf16_f32 v127, v44, v43
	v_cvt_pk_bf16_f32 v128, v48, v47
	v_cvt_pk_bf16_f32 v129, v82, v51
	v_add_f32_e32 v59, v67, v69
	v_add_f32_e32 v1, v58, v1
	v_mfma_f32_32x32x16_bf16 v[20:35], v[126:129], v[200:203], v[20:35]
	v_add_f32_e32 v60, v70, v72
	v_add_f32_e32 v1, v59, v1
	v_add_f32_e32 v61, v71, v73
	v_add_f32_e32 v1, v60, v1
	v_add_f32_e32 v62, v74, v76
	v_add_f32_e32 v1, v61, v1
	s_waitcnt lgkmcnt(0)
	v_mfma_f32_32x32x16_bf16 v[4:19], v[114:117], v[166:169], v[4:19]
	v_add_f32_e32 v63, v75, v77
	v_add_f32_e32 v1, v62, v1
	v_add_f32_e32 v64, v78, v80
	v_add_f32_e32 v1, v63, v1
	v_add_f32_e32 v65, v79, v81
	v_add_f32_e32 v1, v64, v1
	v_mfma_f32_32x32x16_bf16 v[4:19], v[118:121], v[170:173], v[4:19]
	v_add_f32_e32 v1, v65, v1
	v_mov_b32_e32 v2, v1
	s_nop 1
	v_permlane32_swap_b32_e32 v1, v2
	v_add_f32_e32 v1, v1, v2
	v_add_f32_e32 v36, v36, v1
	v_cmp_le_f32_e32 vcc, s0, v36
	v_mfma_f32_32x32x16_bf16 v[4:19], v[122:125], v[174:177], v[4:19]
	v_mfma_f32_32x32x16_bf16 v[4:19], v[126:129], v[178:181], v[4:19]
	s_cmp_eq_u64 vcc, exec
	s_cselect_b64 s[0:1], -1, 0
